# baseline (speedup 1.0000x reference)
.LBB1_28:
	s_or_b64 exec, exec, s[6:7]
	s_load_dwordx2 s[4:5], s[0:1], 0x8
	v_and_b32_e32 v174, 63, v244
	v_lshrrev_b32_e32 v170, 6, v244
	v_mov_b32_e32 v181, 0
	v_lshlrev_b32_e32 v180, 4, v174
	s_waitcnt lgkmcnt(0)
	v_lshl_add_u64 v[0:1], s[4:5], 0, v[180:181]
	v_mul_u32_u24_e32 v120, 0x1800, v170
	v_mov_b32_e32 v121, v181
	s_nop 0
	v_readfirstlane_b32 s82, v170
	s_cmp_eq_u32 s82, 0
	s_cbranch_scc0 .Lwq_full
	v_mul_u32_u24_e32 v122, 0x3000, v170
	v_mov_b32_e32 v123, v181
	v_mul_u32_u24_e32 v182, 0x6000, v170
	v_or_b32_e32 v187, v182, v180
	v_add_u32_e32 v188, 0xf010, v187
	s_nop 0
	v_readfirstlane_b32 s80, v187
	s_add_u32 s80, s80, 0xf010
	s_branch .Lwq_skip
.Lwq_full:
	v_lshl_add_u64 v[2:3], v[0:1], 0, v[120:121]
	v_add_co_u32_e32 v4, vcc, 0x6000, v2
	s_mov_b64 s[4:5], 0x1000
	s_nop 0
	v_addc_co_u32_e32 v5, vcc, 0, v3, vcc
	v_add_co_u32_e32 v110, vcc, 0x1000, v2
	global_load_dwordx4 a[8:11], v[2:3], off
	global_load_dwordx4 a[12:15], v[2:3], off offset:1024
	global_load_dwordx4 a[16:19], v[4:5], off
	global_load_dwordx4 a[20:23], v[4:5], off offset:1024
	global_load_dwordx4 a[24:27], v[2:3], off offset:2048
	global_load_dwordx4 a[28:31], v[2:3], off offset:3072
	global_load_dwordx4 a[32:35], v[4:5], off offset:2048
	global_load_dwordx4 a[36:39], v[4:5], off offset:3072
	v_addc_co_u32_e32 v111, vcc, 0, v3, vcc
	v_add_co_u32_e32 v112, vcc, 0x7000, v2
	v_lshl_add_u64 v[4:5], v[2:3], 0, s[4:5]
	s_nop 0
	v_addc_co_u32_e32 v113, vcc, 0, v3, vcc
	global_load_dwordx4 a[40:43], v[110:111], off
	global_load_dwordx4 a[44:47], v[110:111], off offset:1024
	global_load_dwordx4 a[48:51], v[112:113], off
	global_load_dwordx4 a[52:55], v[112:113], off offset:1024
	v_add_co_u32_e32 v110, vcc, 0x18000, v2
	s_mov_b64 s[4:5], 0x1400
	s_nop 0
	v_addc_co_u32_e32 v111, vcc, 0, v3, vcc
	v_lshl_add_u64 v[114:115], v[2:3], 0, s[4:5]
	v_add_co_u32_e32 v2, vcc, 0x19000, v2
	v_mul_u32_u24_e32 v122, 0x3000, v170
	v_mov_b32_e32 v123, v181
	v_addc_co_u32_e32 v3, vcc, 0, v3, vcc
	v_lshl_add_u64 v[0:1], v[0:1], 0, v[122:123]
	global_load_dwordx4 a[56:59], v[110:111], off
	global_load_dwordx4 a[60:63], v[110:111], off offset:1024
	global_load_dwordx4 a[64:67], v[110:111], off offset:2048
	global_load_dwordx4 a[68:71], v[110:111], off offset:3072
	global_load_dwordx4 a[72:75], v[2:3], off
	global_load_dwordx4 a[76:79], v[2:3], off offset:1024
	v_add_co_u32_e32 v2, vcc, 0x48000, v0
	v_lshl_add_u64 v[144:145], v[4:5], 0, v[120:121]
	s_nop 0
	v_addc_co_u32_e32 v3, vcc, 0, v1, vcc
	global_load_dwordx4 a[80:83], v[2:3], off
	global_load_dwordx4 a[84:87], v[2:3], off offset:1024
	global_load_dwordx4 a[88:91], v[2:3], off offset:2048
	global_load_dwordx4 a[92:95], v[2:3], off offset:3072
	v_add_co_u32_e32 v2, vcc, 0x48000, v144
	v_lshl_add_u64 v[152:153], v[114:115], 0, v[120:121]
	s_nop 0
	v_addc_co_u32_e32 v3, vcc, 0, v145, vcc
	v_add_co_u32_e32 v4, vcc, 0x48000, v152
	s_mov_b32 s3, 0x30000
	s_nop 0
	v_addc_co_u32_e32 v5, vcc, 0, v153, vcc
	global_load_dwordx4 a[96:99], v[2:3], off
	global_load_dwordx4 a[100:103], v[4:5], off
	v_add_co_u32_e32 v2, vcc, 0x49000, v0
	v_mul_u32_u24_e32 v182, 0x6000, v170
	s_nop 0
	v_addc_co_u32_e32 v3, vcc, 0, v1, vcc
	global_load_dwordx4 a[104:107], v[2:3], off offset:2048
	global_load_dwordx4 a[108:111], v[2:3], off offset:3072
	v_add_co_u32_e32 v2, vcc, 0x4a000, v0
	v_or_b32_e32 v187, v182, v180
	s_nop 0
	v_readfirstlane_b32 s80, v187
	s_add_u32 s80, s80, 0xf010
	v_addc_co_u32_e32 v3, vcc, 0, v1, vcc
	v_add_co_u32_e32 v132, vcc, 0x30000, v0
	global_load_dwordx4 a[112:115], v[2:3], off
	global_load_dwordx4 a[116:119], v[2:3], off offset:1024
	global_load_dwordx4 a[120:123], v[2:3], off offset:2048
	global_load_dwordx4 a[124:127], v[2:3], off offset:3072
	v_addc_co_u32_e32 v133, vcc, 0, v1, vcc
	v_add_co_u32_e32 v140, vcc, 0x3c000, v0
	v_add_u32_e32 v188, 0xf010, v187
	s_nop 0
	v_addc_co_u32_e32 v141, vcc, 0, v1, vcc
	v_add_co_u32_e32 v144, vcc, s3, v144
	s_add_u32 m0, s80, 0x0
	s_nop 0
	global_load_lds_dwordx4 v[132:133], off
	s_add_u32 m0, s80, 0x400
	s_nop 0
	global_load_lds_dwordx4 v[132:133], off offset:1024
	s_add_u32 m0, s80, 0x400
	s_nop 0
	global_load_lds_dwordx4 v[140:141], off
	s_add_u32 m0, s80, 0x800
	s_nop 0
	global_load_lds_dwordx4 v[140:141], off offset:1024
	s_add_u32 m0, s80, 0x800
	s_nop 0
	global_load_lds_dwordx4 v[132:133], off offset:2048
	s_nop 0
	s_add_u32 m0, s80, 0xc00
	s_nop 0
	global_load_lds_dwordx4 v[132:133], off offset:3072
	s_nop 0
	s_add_u32 m0, s80, 0xc00
	s_nop 0
	global_load_lds_dwordx4 v[140:141], off offset:2048
	s_nop 0
	s_add_u32 m0, s80, 0x1000
	s_nop 0
	global_load_lds_dwordx4 v[140:141], off offset:3072
	v_addc_co_u32_e32 v145, vcc, 0, v145, vcc
	v_add_co_u32_e32 v168, vcc, 0x3d000, v0
	s_nop 1
	v_addc_co_u32_e32 v169, vcc, 0, v1, vcc
	v_add_co_u32_e32 v172, vcc, s3, v152
	s_add_u32 m0, s80, 0x2000
	s_nop 0
	global_load_lds_dwordx4 v[144:145], off
	s_nop 0
	s_add_u32 m0, s80, 0x2400
	s_nop 0
	global_load_lds_dwordx4 v[168:169], off
	v_addc_co_u32_e32 v173, vcc, 0, v153, vcc
	v_add_co_u32_e32 v164, vcc, 0x31000, v0
	s_nop 1
	v_addc_co_u32_e32 v165, vcc, 0, v1, vcc
	s_add_u32 m0, s80, 0x2800
	s_nop 0
	global_load_lds_dwordx4 v[168:169], off offset:1024
	s_add_u32 m0, s80, 0x2c00
	s_nop 0
	global_load_lds_dwordx4 v[168:169], off offset:2048
	s_add_u32 m0, s80, 0x2800
	s_nop 0
	global_load_lds_dwordx4 v[164:165], off offset:2048
	s_nop 0
	s_add_u32 m0, s80, 0x2c00
	s_nop 0
	global_load_lds_dwordx4 v[164:165], off offset:3072
	s_nop 0
	s_add_u32 m0, s80, 0x2800
	s_nop 0
	global_load_lds_dwordx4 v[172:173], off
	s_add_u32 m0, s80, 0x3000
	s_nop 0
	global_load_lds_dwordx4 v[168:169], off offset:3072
	v_add_co_u32_e32 v168, vcc, 0x32000, v0
	s_nop 1
	v_addc_co_u32_e32 v169, vcc, 0, v1, vcc
	v_add_co_u32_e32 v0, vcc, 0x3e000, v0
	s_nop 1
	v_addc_co_u32_e32 v1, vcc, 0, v1, vcc
	s_add_u32 m0, s80, 0x4000
	s_nop 0
	global_load_lds_dwordx4 v[168:169], off
	s_add_u32 m0, s80, 0x4400
	s_nop 0
	global_load_lds_dwordx4 v[168:169], off offset:1024
	s_add_u32 m0, s80, 0x4400
	s_nop 0
	global_load_lds_dwordx4 v[0:1], off
	s_add_u32 m0, s80, 0x4800
	s_nop 0
	global_load_lds_dwordx4 v[0:1], off offset:1024
	s_add_u32 m0, s80, 0x4800
	s_nop 0
	global_load_lds_dwordx4 v[168:169], off offset:2048
	s_add_u32 m0, s80, 0x4c00
	s_nop 0
	global_load_lds_dwordx4 v[168:169], off offset:3072
	s_add_u32 m0, s80, 0x4c00
	s_nop 0
	global_load_lds_dwordx4 v[0:1], off offset:2048
	s_add_u32 m0, s80, 0x5000
	s_nop 0
	global_load_lds_dwordx4 v[0:1], off offset:3072
.Lwq_skip:
	v_or_b32_e32 v2, 0xffffff00, v244
	v_lshlrev_b32_e32 v3, 4, v244
	s_mov_b64 s[4:5], 0
	v_mov_b32_e32 v110, v181
	v_mov_b32_e32 v111, v181
	v_mov_b32_e32 v112, v181
	v_mov_b32_e32 v113, v181
	s_movk_i32 s3, 0x780

.LBB1_70:
	s_or_b64 exec, exec, s[4:5]
	s_cmp_eq_u32 s82, 0
	s_cbranch_scc0 .Lwq_done
	s_load_dwordx2 s[4:5], s[0:1], 0x8
	v_mov_b32_e32 v8, v180
	v_mov_b32_e32 v9, 0
	s_waitcnt lgkmcnt(0)
	v_lshl_add_u64 v[0:1], s[4:5], 0, v[8:9]
	v_lshl_add_u64 v[2:3], v[0:1], 0, v[120:121]
	v_add_co_u32_e32 v4, vcc, 0x6000, v2
	s_mov_b64 s[4:5], 0x1000
	s_nop 0
	v_addc_co_u32_e32 v5, vcc, 0, v3, vcc
	v_add_co_u32_e32 v10, vcc, 0x1000, v2
	global_load_dwordx4 a[8:11], v[2:3], off
	global_load_dwordx4 a[12:15], v[2:3], off offset:1024
	global_load_dwordx4 a[16:19], v[4:5], off
	global_load_dwordx4 a[20:23], v[4:5], off offset:1024
	global_load_dwordx4 a[24:27], v[2:3], off offset:2048
	global_load_dwordx4 a[28:31], v[2:3], off offset:3072
	global_load_dwordx4 a[32:35], v[4:5], off offset:2048
	global_load_dwordx4 a[36:39], v[4:5], off offset:3072
	v_addc_co_u32_e32 v11, vcc, 0, v3, vcc
	v_add_co_u32_e32 v12, vcc, 0x7000, v2
	v_lshl_add_u64 v[4:5], v[2:3], 0, s[4:5]
	s_nop 0
	v_addc_co_u32_e32 v13, vcc, 0, v3, vcc
	global_load_dwordx4 a[40:43], v[10:11], off
	global_load_dwordx4 a[44:47], v[10:11], off offset:1024
	global_load_dwordx4 a[48:51], v[12:13], off
	global_load_dwordx4 a[52:55], v[12:13], off offset:1024
	v_add_co_u32_e32 v10, vcc, 0x18000, v2
	s_mov_b64 s[4:5], 0x1400
	s_nop 0
	v_addc_co_u32_e32 v11, vcc, 0, v3, vcc
	v_lshl_add_u64 v[14:15], v[2:3], 0, s[4:5]
	v_add_co_u32_e32 v2, vcc, 0x19000, v2
	v_mul_u32_u24_e32 v122, 0x3000, v170
	v_addc_co_u32_e32 v3, vcc, 0, v3, vcc
	v_lshl_add_u64 v[0:1], v[0:1], 0, v[122:123]
	global_load_dwordx4 a[56:59], v[10:11], off
	global_load_dwordx4 a[60:63], v[10:11], off offset:1024
	global_load_dwordx4 a[64:67], v[10:11], off offset:2048
	global_load_dwordx4 a[68:71], v[10:11], off offset:3072
	global_load_dwordx4 a[72:75], v[2:3], off
	global_load_dwordx4 a[76:79], v[2:3], off offset:1024
	v_add_co_u32_e32 v2, vcc, 0x48000, v0
	v_lshl_add_u64 v[144:145], v[4:5], 0, v[120:121]
	s_nop 0
	v_addc_co_u32_e32 v3, vcc, 0, v1, vcc
	global_load_dwordx4 a[80:83], v[2:3], off
	global_load_dwordx4 a[84:87], v[2:3], off offset:1024
	global_load_dwordx4 a[88:91], v[2:3], off offset:2048
	global_load_dwordx4 a[92:95], v[2:3], off offset:3072
	v_add_co_u32_e32 v2, vcc, 0x48000, v144
	v_lshl_add_u64 v[152:153], v[14:15], 0, v[120:121]
	s_nop 0
	v_addc_co_u32_e32 v3, vcc, 0, v145, vcc
	v_add_co_u32_e32 v4, vcc, 0x48000, v152
	s_mov_b32 s3, 0x30000
	s_nop 0
	v_addc_co_u32_e32 v5, vcc, 0, v153, vcc
	global_load_dwordx4 a[96:99], v[2:3], off
	global_load_dwordx4 a[100:103], v[4:5], off
	v_add_co_u32_e32 v2, vcc, 0x49000, v0
	v_mul_u32_u24_e32 v182, 0x6000, v170
	s_nop 0
	v_addc_co_u32_e32 v3, vcc, 0, v1, vcc
	global_load_dwordx4 a[104:107], v[2:3], off offset:2048
	global_load_dwordx4 a[108:111], v[2:3], off offset:3072
	v_add_co_u32_e32 v2, vcc, 0x4a000, v0
	v_or_b32_e32 v187, v182, v180
	s_nop 0
	v_readfirstlane_b32 s80, v187
	s_add_u32 s80, s80, 0xf010
	v_addc_co_u32_e32 v3, vcc, 0, v1, vcc
	v_add_co_u32_e32 v132, vcc, 0x30000, v0
	global_load_dwordx4 a[112:115], v[2:3], off
	global_load_dwordx4 a[116:119], v[2:3], off offset:1024
	global_load_dwordx4 a[120:123], v[2:3], off offset:2048
	global_load_dwordx4 a[124:127], v[2:3], off offset:3072
	v_addc_co_u32_e32 v133, vcc, 0, v1, vcc
	v_add_co_u32_e32 v140, vcc, 0x3c000, v0
	v_add_u32_e32 v188, 0xf010, v187
	s_nop 0
	v_addc_co_u32_e32 v141, vcc, 0, v1, vcc
	v_add_co_u32_e32 v144, vcc, s3, v144
	s_add_u32 m0, s80, 0x0
	s_nop 0
	global_load_lds_dwordx4 v[132:133], off
	s_add_u32 m0, s80, 0x400
	s_nop 0
	global_load_lds_dwordx4 v[132:133], off offset:1024
	s_add_u32 m0, s80, 0x400
	s_nop 0
	global_load_lds_dwordx4 v[140:141], off
	s_add_u32 m0, s80, 0x800
	s_nop 0
	global_load_lds_dwordx4 v[140:141], off offset:1024
	s_add_u32 m0, s80, 0x800
	s_nop 0
	global_load_lds_dwordx4 v[132:133], off offset:2048
	s_nop 0
	s_add_u32 m0, s80, 0xc00
	s_nop 0
	global_load_lds_dwordx4 v[132:133], off offset:3072
	s_nop 0
	s_add_u32 m0, s80, 0xc00
	s_nop 0
	global_load_lds_dwordx4 v[140:141], off offset:2048
	s_nop 0
	s_add_u32 m0, s80, 0x1000
	s_nop 0
	global_load_lds_dwordx4 v[140:141], off offset:3072
	v_addc_co_u32_e32 v145, vcc, 0, v145, vcc
	v_add_co_u32_e32 v168, vcc, 0x3d000, v0
	s_nop 1
	v_addc_co_u32_e32 v169, vcc, 0, v1, vcc
	v_add_co_u32_e32 v172, vcc, s3, v152
	s_add_u32 m0, s80, 0x2000
	s_nop 0
	global_load_lds_dwordx4 v[144:145], off
	s_nop 0
	s_add_u32 m0, s80, 0x2400
	s_nop 0
	global_load_lds_dwordx4 v[168:169], off
	v_addc_co_u32_e32 v173, vcc, 0, v153, vcc
	v_add_co_u32_e32 v164, vcc, 0x31000, v0
	s_nop 1
	v_addc_co_u32_e32 v165, vcc, 0, v1, vcc
	s_add_u32 m0, s80, 0x2800
	s_nop 0
	global_load_lds_dwordx4 v[168:169], off offset:1024
	s_add_u32 m0, s80, 0x2c00
	s_nop 0
	global_load_lds_dwordx4 v[168:169], off offset:2048
	s_add_u32 m0, s80, 0x2800
	s_nop 0
	global_load_lds_dwordx4 v[164:165], off offset:2048
	s_nop 0
	s_add_u32 m0, s80, 0x2c00
	s_nop 0
	global_load_lds_dwordx4 v[164:165], off offset:3072
	s_nop 0
	s_add_u32 m0, s80, 0x2800
	s_nop 0
	global_load_lds_dwordx4 v[172:173], off
	s_add_u32 m0, s80, 0x3000
	s_nop 0
	global_load_lds_dwordx4 v[168:169], off offset:3072
	v_add_co_u32_e32 v168, vcc, 0x32000, v0
	s_nop 1
	v_addc_co_u32_e32 v169, vcc, 0, v1, vcc
	v_add_co_u32_e32 v0, vcc, 0x3e000, v0
	s_nop 1
	v_addc_co_u32_e32 v1, vcc, 0, v1, vcc
	s_add_u32 m0, s80, 0x4000
	s_nop 0
	global_load_lds_dwordx4 v[168:169], off
	s_add_u32 m0, s80, 0x4400
	s_nop 0
	global_load_lds_dwordx4 v[168:169], off offset:1024
	s_add_u32 m0, s80, 0x4400
	s_nop 0
	global_load_lds_dwordx4 v[0:1], off
	s_add_u32 m0, s80, 0x4800
	s_nop 0
	global_load_lds_dwordx4 v[0:1], off offset:1024
	s_add_u32 m0, s80, 0x4800
	s_nop 0
	global_load_lds_dwordx4 v[168:169], off offset:2048
	s_add_u32 m0, s80, 0x4c00
	s_nop 0
	global_load_lds_dwordx4 v[168:169], off offset:3072
	s_add_u32 m0, s80, 0x4c00
	s_nop 0
	global_load_lds_dwordx4 v[0:1], off offset:2048
	s_add_u32 m0, s80, 0x5000
	s_nop 0
	global_load_lds_dwordx4 v[0:1], off offset:3072
.Lwq_done:
	v_cmp_gt_u32_e64 s[2:3], 32, v244
	v_mov_b32_e32 v59, 0
	v_mov_b32_e32 v6, 0
	s_waitcnt lgkmcnt(0)
	s_barrier
	s_and_saveexec_b64 s[4:5], s[2:3]
	v_mov_b32_e32 v0, 0x27610
	v_lshl_add_u32 v0, v244, 2, v0
	ds_read_b32 v6, v0
	s_or_b64 exec, exec, s[4:5]
	s_load_dwordx4 s[12:15], s[0:1], 0x8
	s_load_dwordx4 s[16:19], s[0:1], 0x58
	v_lshlrev_b32_e32 v60, 2, v244
	s_cmp_lg_u32 s7, 0
	v_add_u32_e32 v0, 0x27690, v60
	v_lshlrev_b32_e32 v58, 4, v174
	s_cselect_b64 s[28:29], -1, 0
	s_cmp_lg_u32 s6, 0
	v_accvgpr_write_b32 a143, v0
	s_waitcnt lgkmcnt(0)
	v_lshl_add_u64 v[0:1], s[12:13], 0, v[58:59]
	s_mov_b64 s[6:7], 0x60000
	v_lshl_add_u64 v[0:1], v[0:1], 0, s[6:7]
	v_lshl_add_u64 v[62:63], v[0:1], 0, v[120:121]
	s_mov_b64 s[6:7], 0x6000
	v_lshl_add_u64 v[2:3], v[62:63], 0, s[6:7]
	v_accvgpr_write_b32 a147, v3
	s_mov_b64 s[6:7], 0x6400
	v_accvgpr_write_b32 a146, v2
	v_lshl_add_u64 v[2:3], v[62:63], 0, s[6:7]
	v_accvgpr_write_b32 a149, v3
	s_mov_b64 s[6:7], 0x6800
	v_accvgpr_write_b32 a148, v2
	v_lshl_add_u64 v[2:3], v[62:63], 0, s[6:7]
	v_accvgpr_write_b32 a151, v3
	s_mov_b64 s[6:7], 0x6c00
	v_accvgpr_write_b32 a150, v2
	v_lshl_add_u64 v[2:3], v[62:63], 0, s[6:7]
	s_mov_b64 s[6:7], 0x1000
	v_accvgpr_write_b32 a153, v3
	v_lshl_add_u64 v[222:223], v[62:63], 0, s[6:7]
	s_mov_b64 s[6:7], 0x7000
	v_accvgpr_write_b32 a152, v2
	v_lshl_add_u64 v[2:3], v[62:63], 0, s[6:7]
	s_mov_b64 s[6:7], 0x1400
	v_accvgpr_write_b32 a155, v3
	v_lshl_add_u64 v[76:77], v[62:63], 0, s[6:7]
	s_mov_b64 s[6:7], 0x7400
	v_accvgpr_write_b32 a154, v2
	v_lshl_add_u64 v[2:3], v[62:63], 0, s[6:7]
	v_accvgpr_write_b32 a157, v3
	s_mov_b64 s[6:7], 0x18000
	v_accvgpr_write_b32 a156, v2
	v_lshl_add_u64 v[2:3], v[62:63], 0, s[6:7]
	v_accvgpr_write_b32 a159, v3
	s_mov_b64 s[6:7], 0x18400
	v_accvgpr_write_b32 a158, v2
	v_lshl_add_u64 v[2:3], v[62:63], 0, s[6:7]
	v_accvgpr_write_b32 a161, v3
	s_mov_b64 s[6:7], 0x18800
	v_accvgpr_write_b32 a160, v2
	v_lshl_add_u64 v[2:3], v[62:63], 0, s[6:7]
	v_accvgpr_write_b32 a163, v3
	s_mov_b64 s[6:7], 0x18c00
	v_accvgpr_write_b32 a162, v2
	v_lshl_add_u64 v[2:3], v[62:63], 0, s[6:7]
	v_accvgpr_write_b32 a165, v3
	s_mov_b64 s[6:7], 0x19000
	v_accvgpr_write_b32 a164, v2
	v_lshl_add_u64 v[2:3], v[62:63], 0, s[6:7]
	v_accvgpr_write_b32 a167, v3
	s_mov_b64 s[6:7], 0x19400
	v_accvgpr_write_b32 a166, v2
	v_lshl_add_u64 v[2:3], v[62:63], 0, s[6:7]
	v_accvgpr_write_b32 a169, v3
	v_lshl_add_u64 v[0:1], v[0:1], 0, v[122:123]
	s_mov_b64 s[6:7], 0x48000
	v_accvgpr_write_b32 a168, v2
	v_lshl_add_u64 v[2:3], v[0:1], 0, s[6:7]
	v_accvgpr_write_b32 a171, v3
	s_mov_b64 s[8:9], 0x48400
	v_accvgpr_write_b32 a170, v2
	v_lshl_add_u64 v[2:3], v[0:1], 0, s[8:9]
	v_accvgpr_write_b32 a173, v3
	s_mov_b64 s[8:9], 0x48800
	v_accvgpr_write_b32 a172, v2
	v_lshl_add_u64 v[2:3], v[0:1], 0, s[8:9]
	v_accvgpr_write_b32 a175, v3
	s_mov_b64 s[8:9], 0x48c00
	v_accvgpr_write_b32 a174, v2
	v_lshl_add_u64 v[2:3], v[0:1], 0, s[8:9]
	v_accvgpr_write_b32 a177, v3
	v_accvgpr_write_b32 a176, v2
	v_lshl_add_u64 v[2:3], v[222:223], 0, v[120:121]
	v_lshl_add_u64 v[4:5], v[2:3], 0, s[6:7]
	v_accvgpr_write_b32 a179, v5
	v_accvgpr_write_b32 a178, v4
	v_lshl_add_u64 v[4:5], v[76:77], 0, v[120:121]
	v_lshl_add_u64 v[8:9], v[4:5], 0, s[6:7]
	v_accvgpr_write_b32 a181, v9
	s_mov_b64 s[6:7], 0x49800
	v_accvgpr_write_b32 a180, v8
	v_lshl_add_u64 v[8:9], v[0:1], 0, s[6:7]
	v_accvgpr_write_b32 a183, v9
	s_mov_b64 s[6:7], 0x49c00
	v_accvgpr_write_b32 a182, v8
	v_lshl_add_u64 v[8:9], v[0:1], 0, s[6:7]
	v_accvgpr_write_b32 a185, v9
	s_mov_b64 s[6:7], 0x4a000
	v_accvgpr_write_b32 a184, v8
	v_lshl_add_u64 v[8:9], v[0:1], 0, s[6:7]
	v_accvgpr_write_b32 a187, v9
	s_mov_b64 s[6:7], 0x4a400
	v_accvgpr_write_b32 a186, v8
	v_lshl_add_u64 v[8:9], v[0:1], 0, s[6:7]
	v_accvgpr_write_b32 a189, v9
	s_mov_b64 s[6:7], 0x4a800
	v_accvgpr_write_b32 a188, v8
	v_lshl_add_u64 v[8:9], v[0:1], 0, s[6:7]
	v_accvgpr_write_b32 a191, v9
	s_mov_b64 s[6:7], 0x4ac00
	v_accvgpr_write_b32 a190, v8
	v_lshl_add_u64 v[8:9], v[0:1], 0, s[6:7]
	v_accvgpr_write_b32 a193, v9
	s_mov_b64 s[6:7], 0x30000
	v_accvgpr_write_b32 a192, v8
	v_lshl_add_u64 v[8:9], v[0:1], 0, s[6:7]
	v_accvgpr_write_b32 a195, v9
	s_mov_b64 s[8:9], 0x3c000
	v_accvgpr_write_b32 a194, v8
	v_lshl_add_u64 v[8:9], v[0:1], 0, s[8:9]
	v_accvgpr_write_b32 a197, v9
	s_mov_b64 s[8:9], 0x30400
	v_accvgpr_write_b32 a196, v8
	v_lshl_add_u64 v[8:9], v[0:1], 0, s[8:9]
	v_accvgpr_write_b32 a199, v9
	s_mov_b64 s[8:9], 0x3c400
	v_accvgpr_write_b32 a198, v8
	v_lshl_add_u64 v[8:9], v[0:1], 0, s[8:9]
	v_accvgpr_write_b32 a201, v9
	s_mov_b64 s[8:9], 0x30800
	v_accvgpr_write_b32 a200, v8
	v_lshl_add_u64 v[8:9], v[0:1], 0, s[8:9]
	v_accvgpr_write_b32 a203, v9
	s_mov_b64 s[8:9], 0x3c800
	v_accvgpr_write_b32 a202, v8
	v_lshl_add_u64 v[8:9], v[0:1], 0, s[8:9]
	v_accvgpr_write_b32 a205, v9
	s_mov_b64 s[8:9], 0x30c00
	v_accvgpr_write_b32 a204, v8
	v_lshl_add_u64 v[8:9], v[0:1], 0, s[8:9]
	v_accvgpr_write_b32 a207, v9
	s_mov_b64 s[8:9], 0x3cc00
	v_lshl_add_u64 v[2:3], v[2:3], 0, s[6:7]
	v_accvgpr_write_b32 a206, v8
	v_lshl_add_u64 v[8:9], v[0:1], 0, s[8:9]
	v_accvgpr_write_b32 a211, v3
	s_mov_b64 s[8:9], 0x3d000
	v_accvgpr_write_b32 a210, v2
	v_lshl_add_u64 v[2:3], v[0:1], 0, s[8:9]
	v_accvgpr_write_b32 a213, v3
	v_accvgpr_write_b32 a212, v2
	v_lshl_add_u64 v[2:3], v[4:5], 0, s[6:7]
	v_accvgpr_write_b32 a215, v3
	s_mov_b64 s[6:7], 0x3d400
	v_accvgpr_write_b32 a214, v2
	v_lshl_add_u64 v[2:3], v[0:1], 0, s[6:7]
	v_accvgpr_write_b32 a217, v3
	s_mov_b64 s[6:7], 0x31800
	v_accvgpr_write_b32 a216, v2
	v_lshl_add_u64 v[2:3], v[0:1], 0, s[6:7]
	v_accvgpr_write_b32 a219, v3
	s_mov_b64 s[6:7], 0x3d800
	v_accvgpr_write_b32 a218, v2
	v_lshl_add_u64 v[2:3], v[0:1], 0, s[6:7]
	v_accvgpr_write_b32 a221, v3
	s_mov_b64 s[6:7], 0x31c00
	v_accvgpr_write_b32 a220, v2
	v_lshl_add_u64 v[2:3], v[0:1], 0, s[6:7]
	v_accvgpr_write_b32 a223, v3
	s_mov_b64 s[6:7], 0x3dc00
	v_accvgpr_write_b32 a222, v2
	v_lshl_add_u64 v[2:3], v[0:1], 0, s[6:7]
	v_accvgpr_write_b32 a225, v3
	s_mov_b64 s[6:7], 0x32000
	v_accvgpr_write_b32 a224, v2
	v_lshl_add_u64 v[2:3], v[0:1], 0, s[6:7]
	v_accvgpr_write_b32 a227, v3
	s_mov_b64 s[6:7], 0x3e000
	v_accvgpr_write_b32 a226, v2
	v_lshl_add_u64 v[2:3], v[0:1], 0, s[6:7]
	v_accvgpr_write_b32 a229, v3
	s_mov_b64 s[6:7], 0x32400
	v_accvgpr_write_b32 a228, v2
	v_lshl_add_u64 v[2:3], v[0:1], 0, s[6:7]
	v_accvgpr_write_b32 a231, v3
	s_mov_b64 s[6:7], 0x3e400
	v_accvgpr_write_b32 a230, v2
	v_lshl_add_u64 v[2:3], v[0:1], 0, s[6:7]
	v_accvgpr_write_b32 a233, v3
	s_mov_b64 s[6:7], 0x32800
	v_accvgpr_write_b32 a232, v2
	v_lshl_add_u64 v[2:3], v[0:1], 0, s[6:7]
	v_accvgpr_write_b32 a235, v3
	s_mov_b64 s[6:7], 0x3e800
	v_accvgpr_write_b32 a234, v2
	v_lshl_add_u64 v[2:3], v[0:1], 0, s[6:7]
	s_mov_b64 s[6:7], 0x32c00
	s_mul_hi_u32 s4, s26, 0x13b13b14
	v_lshl_add_u64 v[4:5], v[0:1], 0, s[6:7]
	s_mov_b64 s[6:7], 0x3ec00
	s_mul_i32 s4, s4, 13
	v_lshl_add_u64 v[166:167], v[0:1], 0, s[6:7]
	s_load_dwordx2 s[6:7], s[0:1], 0x70
	s_cselect_b64 s[30:31], -1, 0
	s_sub_i32 s4, s26, s4
	v_lshlrev_b32_e32 v0, 7, v170
	s_add_i32 s5, s4, 1
	s_add_i32 s12, s4, 2
	s_add_i32 s34, s4, 3
	s_add_i32 s37, s4, 4
	s_add_i32 s40, s4, 5
	s_add_i32 s43, s4, 6
	s_add_i32 s46, s4, 7
	s_add_i32 s49, s4, 8
	s_add_i32 s52, s4, 9
	s_add_i32 s55, s4, 10
	s_add_i32 s58, s4, 11
	s_add_i32 s61, s4, 12
	v_lshl_or_b32 v58, s33, 9, v0
	s_lshl_b32 s10, s5, 10
	s_lshl_b32 s13, s12, 10
	s_lshl_b32 s35, s34, 10
	s_lshl_b32 s38, s37, 10
	s_lshl_b32 s41, s40, 10
	s_lshl_b32 s44, s43, 10
	s_lshl_b32 s47, s46, 10
	s_lshl_b32 s50, s49, 10
	s_lshl_b32 s53, s52, 10
	s_lshl_b32 s56, s55, 10
	s_lshl_b32 s59, s58, 10
	s_lshl_b32 s8, s61, 10
	s_mov_b32 s27, 0
	s_lshl_b32 s24, s26, 4
	v_accvgpr_write_b32 a145, v0
	v_lshl_add_u64 v[0:1], s[18:19], 0, v[58:59]
	s_lshl_b32 s18, s4, 10
	s_add_i32 s11, s10, 0xffffcc00
	s_add_i32 s19, s13, 0xffffcc00
	s_add_i32 s36, s35, 0xffffcc00
	s_add_i32 s39, s38, 0xffffcc00
	s_add_i32 s42, s41, 0xffffcc00
	s_add_i32 s45, s44, 0xffffcc00
	s_add_i32 s48, s47, 0xffffcc00
	s_add_i32 s51, s50, 0xffffcc00
	s_add_i32 s54, s53, 0xffffcc00
	s_add_i32 s57, s56, 0xffffcc00
	s_add_i32 s60, s59, 0xffffcc00
	s_add_i32 s62, s8, 0xffffcc00
	s_mul_i32 s8, s33, 0x640
	s_mov_b32 s25, s27
	s_waitcnt lgkmcnt(0)
	s_add_u32 s8, s6, s8
	s_addc_u32 s9, s7, 0
	s_lshl_b64 s[6:7], s[24:25], 2
	s_add_u32 s8, s8, s6
	s_addc_u32 s9, s9, s7
	s_lshl_b32 s5, s5, 6
	s_add_i32 s6, s5, 0xfffffcc0
	s_cmp_gt_u32 s4, 11
	s_cselect_b32 s25, s11, s10
	s_cselect_b32 s10, s6, s5
	s_lshl_b32 s5, s12, 6
	s_add_i32 s6, s5, 0xfffffcc0
	s_cmp_gt_u32 s4, 10
	s_cselect_b32 s19, s19, s13
	s_cselect_b32 s11, s6, s5
	s_lshl_b32 s5, s34, 6
	s_add_i32 s6, s5, 0xfffffcc0
	s_cmp_gt_u32 s4, 9
	s_cselect_b32 s34, s36, s35
	s_cselect_b32 s12, s6, s5
	s_lshl_b32 s5, s37, 6
	s_add_i32 s6, s5, 0xfffffcc0
	s_cmp_gt_u32 s4, 8
	s_cselect_b32 s35, s39, s38
	s_cselect_b32 s13, s6, s5
	s_lshl_b32 s5, s40, 6
	s_add_i32 s6, s5, 0xfffffcc0
	s_cmp_gt_u32 s4, 7
	s_cselect_b32 s36, s42, s41
	s_cselect_b32 s37, s6, s5
	s_lshl_b32 s5, s43, 6
	s_add_i32 s6, s5, 0xfffffcc0
	s_cmp_gt_u32 s4, 6
	s_cselect_b32 s38, s45, s44
	s_cselect_b32 s39, s6, s5
	s_lshl_b32 s5, s46, 6
	s_add_i32 s6, s5, 0xfffffcc0
	s_cmp_gt_u32 s4, 5
	s_cselect_b32 s40, s48, s47
	s_cselect_b32 s41, s6, s5
	s_lshl_b32 s5, s49, 6
	s_add_i32 s6, s5, 0xfffffcc0
	s_cmp_gt_u32 s4, 4
	s_cselect_b32 s42, s51, s50
	s_cselect_b32 s43, s6, s5
	s_lshl_b32 s5, s52, 6
	s_add_i32 s6, s5, 0xfffffcc0
	s_cmp_gt_u32 s4, 3
	s_cselect_b32 s44, s54, s53
	s_cselect_b32 s45, s6, s5
	s_lshl_b32 s5, s55, 6
	s_add_i32 s6, s5, 0xfffffcc0
	s_cmp_gt_u32 s4, 2
	s_cselect_b32 s46, s57, s56
	s_cselect_b32 s47, s6, s5
	s_lshl_b32 s5, s58, 6
	s_add_i32 s6, s5, 0xfffffcc0
	s_cmp_gt_u32 s4, 1
	v_accvgpr_write_b32 a209, v9
	v_accvgpr_write_b32 a237, v3
	s_cselect_b32 s48, s60, s59
	s_cselect_b32 s49, s6, s5
	s_lshl_b32 s5, s61, 6
	v_accvgpr_write_b32 a208, v8
	v_accvgpr_write_b32 a236, v2
	v_min_u32_e32 v2, 24, v174
	v_lshl_or_b32 v8, s33, 2, v170
	s_add_i32 s50, s5, 0xfffffcc0
	v_lshlrev_b32_e32 v58, 2, v2
	v_mul_u32_u24_e32 v2, 0x3400, v8
	s_cmp_eq_u32 s4, 0
	v_or_b32_e32 v2, v2, v180
	s_cselect_b32 s51, 0x3000, s62
	v_mov_b32_e32 v61, v59
	s_waitcnt vmcnt(0)
	v_accvgpr_read_b32 v3, a142
	v_lshlrev_b32_e32 v7, 2, v183
	v_add_u32_e32 v194, s18, v2
	v_add_u32_e32 v195, s25, v2
	v_add_u32_e32 v196, s19, v2
	v_add_u32_e32 v197, s34, v2
	v_add_u32_e32 v198, s35, v2
	v_add_u32_e32 v199, s36, v2
	v_add_u32_e32 v200, s38, v2
	v_add_u32_e32 v201, s40, v2
	v_add_u32_e32 v202, s42, v2
	v_add_u32_e32 v203, s44, v2
	v_add_u32_e32 v204, s46, v2
	v_add_u32_e32 v205, s48, v2
	v_add_u32_e32 v206, s51, v2
	v_lshl_add_u64 v[170:171], s[8:9], 0, v[60:61]
	v_lshl_or_b32 v213, s37, 4, v180
	s_cselect_b32 s8, 0x300, s50
	v_and_b32_e32 v2, 16, v244
	v_mul_f32_e32 v3, v3, v6
	v_or_b32_e32 v6, s24, v181
	v_or_b32_e32 v11, 32, v8
	s_bfe_u32 s37, s26, 0x1b0001
	v_lshl_add_u64 v[168:169], v[0:1], 0, v[58:59]
	v_lshl_or_b32 v2, v2, 2, v7
	v_mad_u32_u24 v58, v11, 13, s37
	v_lshlrev_b32_e32 v6, 1, v6
	v_accvgpr_write_b32 a238, v3
	v_accvgpr_write_b32 a239, v2
	v_lshlrev_b64 v[2:3], 10, v[58:59]
	v_and_or_b32 v6, v6, 48, v183
	v_lshl_add_u64 v[2:3], s[16:17], 0, v[2:3]
	v_lshlrev_b32_e32 v58, 4, v6
	v_and_b32_e32 v6, 4, v111
	v_accvgpr_write_b32 a144, v7
	v_lshl_add_u64 v[2:3], v[2:3], 0, v[58:59]
	v_lshlrev_b32_e32 v6, 1, v6
	v_mov_b32_e32 v7, v59
	s_lshl_b32 s26, s26, 2
	v_lshl_or_b32 v209, s10, 4, v180
	v_lshl_or_b32 v210, s11, 4, v180
	v_lshl_or_b32 v211, s12, 4, v180
	v_lshl_or_b32 v212, s13, 4, v180
	v_cmp_gt_u32_e64 s[10:11], 16, v174
	v_lshl_add_u64 v[172:173], v[2:3], 0, v[6:7]
	v_lshlrev_b32_e32 v2, 1, v175
	v_cmp_eq_u32_e64 s[12:13], 0, v174
	v_lshl_add_u64 v[174:175], v[0:1], 0, s[26:27]
	v_mul_u32_u24_e32 v0, 0x3400, v11
	v_or_b32_e32 v0, v0, v180
	v_add_u32_e32 v229, s18, v0
	v_add_u32_e32 v230, s25, v0
	v_add_u32_e32 v231, s19, v0
	v_add_u32_e32 v232, s34, v0
	v_add_u32_e32 v233, s35, v0
	v_add_u32_e32 v234, s36, v0
	v_add_u32_e32 v235, s38, v0
	v_add_u32_e32 v236, s40, v0
	v_add_u32_e32 v237, s42, v0
	v_add_u32_e32 v238, s44, v0
	v_add_u32_e32 v239, s46, v0
	v_add_u32_e32 v240, s48, v0
	v_add_u32_e32 v241, s51, v0
	v_add_u32_e32 v1, 0x3000, v0
	v_add_u32_e32 v9, 0xfff98000, v1
	v_and_b32_e32 v10, 0x200, v180
	v_cmp_eq_u32_e32 vcc, v9, v194
	s_nop 1
	v_cndmask_b32_e32 v12, 0, v10, vcc
	v_sub_u32_e32 v194, v194, v12
	v_cmp_eq_u32_e32 vcc, v9, v195
	s_nop 1
	v_cndmask_b32_e32 v12, 0, v10, vcc
	v_sub_u32_e32 v195, v195, v12
	v_cmp_eq_u32_e32 vcc, v9, v196
	s_nop 1
	v_cndmask_b32_e32 v12, 0, v10, vcc
	v_sub_u32_e32 v196, v196, v12
	v_cmp_eq_u32_e32 vcc, v9, v197
	s_nop 1
	v_cndmask_b32_e32 v12, 0, v10, vcc
	v_sub_u32_e32 v197, v197, v12
	v_cmp_eq_u32_e32 vcc, v9, v198
	s_nop 1
	v_cndmask_b32_e32 v12, 0, v10, vcc
	v_sub_u32_e32 v198, v198, v12
	v_cmp_eq_u32_e32 vcc, v9, v199
	s_nop 1
	v_cndmask_b32_e32 v12, 0, v10, vcc
	v_sub_u32_e32 v199, v199, v12
	v_cmp_eq_u32_e32 vcc, v9, v200
	s_nop 1
	v_cndmask_b32_e32 v12, 0, v10, vcc
	v_sub_u32_e32 v200, v200, v12
	v_cmp_eq_u32_e32 vcc, v9, v201
	s_nop 1
	v_cndmask_b32_e32 v12, 0, v10, vcc
	v_sub_u32_e32 v201, v201, v12
	v_cmp_eq_u32_e32 vcc, v9, v202
	s_nop 1
	v_cndmask_b32_e32 v12, 0, v10, vcc
	v_sub_u32_e32 v202, v202, v12
	v_cmp_eq_u32_e32 vcc, v9, v203
	s_nop 1
	v_cndmask_b32_e32 v12, 0, v10, vcc
	v_sub_u32_e32 v203, v203, v12
	v_cmp_eq_u32_e32 vcc, v9, v204
	s_nop 1
	v_cndmask_b32_e32 v12, 0, v10, vcc
	v_sub_u32_e32 v204, v204, v12
	v_cmp_eq_u32_e32 vcc, v9, v205
	s_nop 1
	v_cndmask_b32_e32 v12, 0, v10, vcc
	v_sub_u32_e32 v205, v205, v12
	v_cmp_eq_u32_e32 vcc, v9, v206
	s_nop 1
	v_cndmask_b32_e32 v12, 0, v10, vcc
	v_sub_u32_e32 v206, v206, v12
	v_cmp_eq_u32_e32 vcc, v1, v229
	s_nop 1
	v_cndmask_b32_e32 v12, 0, v10, vcc
	v_sub_u32_e32 v229, v229, v12
	v_cmp_eq_u32_e32 vcc, v1, v230
	s_nop 1
	v_cndmask_b32_e32 v12, 0, v10, vcc
	v_sub_u32_e32 v230, v230, v12
	v_cmp_eq_u32_e32 vcc, v1, v231
	s_nop 1
	v_cndmask_b32_e32 v12, 0, v10, vcc
	v_sub_u32_e32 v231, v231, v12
	v_cmp_eq_u32_e32 vcc, v1, v232
	s_nop 1
	v_cndmask_b32_e32 v12, 0, v10, vcc
	v_sub_u32_e32 v232, v232, v12
	v_cmp_eq_u32_e32 vcc, v1, v233
	s_nop 1
	v_cndmask_b32_e32 v12, 0, v10, vcc
	v_sub_u32_e32 v233, v233, v12
	v_cmp_eq_u32_e32 vcc, v1, v234
	s_nop 1
	v_cndmask_b32_e32 v12, 0, v10, vcc
	v_sub_u32_e32 v234, v234, v12
	v_cmp_eq_u32_e32 vcc, v1, v235
	s_nop 1
	v_cndmask_b32_e32 v12, 0, v10, vcc
	v_sub_u32_e32 v235, v235, v12
	v_cmp_eq_u32_e32 vcc, v1, v236
	s_nop 1
	v_cndmask_b32_e32 v12, 0, v10, vcc
	v_sub_u32_e32 v236, v236, v12
	v_cmp_eq_u32_e32 vcc, v1, v237
	s_nop 1
	v_cndmask_b32_e32 v12, 0, v10, vcc
	v_sub_u32_e32 v237, v237, v12
	v_cmp_eq_u32_e32 vcc, v1, v238
	s_nop 1
	v_cndmask_b32_e32 v12, 0, v10, vcc
	v_sub_u32_e32 v238, v238, v12
	v_cmp_eq_u32_e32 vcc, v1, v239
	s_nop 1
	v_cndmask_b32_e32 v12, 0, v10, vcc
	v_sub_u32_e32 v239, v239, v12
	v_cmp_eq_u32_e32 vcc, v1, v240
	s_nop 1
	v_cndmask_b32_e32 v12, 0, v10, vcc
	v_sub_u32_e32 v240, v240, v12
	v_cmp_eq_u32_e32 vcc, v1, v241
	s_nop 1
	v_cndmask_b32_e32 v12, 0, v10, vcc
	v_sub_u32_e32 v241, v241, v12
	v_mad_u32_u24 v0, v8, 13, s37
	v_mov_b32_e32 v1, v59
	v_lshlrev_b64 v[0:1], 10, v[0:1]
	v_lshl_add_u64 v[0:1], s[16:17], 0, v[0:1]
	v_mov_b32_e32 v111, v59
	v_lshl_add_u64 v[0:1], v[0:1], 0, v[58:59]
	v_mul_u32_u24_e32 v61, 0x320, v183
	v_lshlrev_b32_e32 v9, 1, v113
	v_lshlrev_b32_e32 v10, 1, v181
	v_lshlrev_b32_e32 v225, 2, v181
	v_lshl_add_u64 v[176:177], s[14:15], 0, v[110:111]
	v_mul_u32_u24_e32 v111, 0x220, v183
	v_lshl_add_u64 v[178:179], v[0:1], 0, v[6:7]
	v_mul_u32_u24_e32 v0, 0x320, v181
	s_movk_i32 s52, 0x320
	v_add3_u32 v221, v61, v9, v10
	v_lshlrev_b32_e32 v224, 8, v181
	v_sub_u32_e32 v3, v110, v2
	v_mul_u32_u24_e32 v12, 0x220, v181
	v_add3_u32 v9, v111, v9, v10
	s_mov_b32 s14, 0xf010
	v_lshl_add_u32 v1, v113, 2, v225
	v_add_u32_e32 v245, v2, v0
	v_mbcnt_lo_u32_b32 v0, -1, 0
	v_add_u32_e32 v189, 0x27010, v60
	v_cmp_lt_u32_e64 s[4:5], 15, v244
	v_cmp_gt_u32_e64 s[6:7], 16, v244
	v_and_b32_e32 v207, 48, v244
	v_or_b32_e32 v208, s18, v180
	v_lshl_or_b32 v214, s39, 4, v180
	v_lshl_or_b32 v215, s41, 4, v180
	v_lshl_or_b32 v216, s43, 4, v180
	v_lshl_or_b32 v217, s45, 4, v180
	v_lshl_or_b32 v218, s47, 4, v180
	v_lshl_or_b32 v219, s49, 4, v180
	v_lshl_or_b32 v220, s8, 4, v180
	v_cmp_gt_u32_e64 s[8:9], 48, v244
	v_or_b32_e32 v226, 0x100, v224
	v_or_b32_e32 v227, 0x200, v224
	v_or_b32_e32 v228, 0x300, v224
	v_or_b32_e32 v242, v224, v110
	v_add3_u32 v58, v180, v182, s14
	v_mad_u32_u24 v243, v181, s52, v2
	v_accvgpr_write_b32 a136, v183
	v_cmp_eq_u32_e64 s[14:15], 0, v183
	v_accvgpr_write_b32 a240, v1
	v_mov_b32_e32 v113, v112
	v_mbcnt_hi_u32_b32 v246, -1, v0
	v_add_u32_e32 v247, v3, v12
	v_add_u32_e32 v248, 0x3000, v9
	s_mov_b32 s25, 0
	s_mov_b32 s64, 0x40004000
	s_mov_b32 s65, 0
	s_mov_b32 s71, 0
	s_mov_b32 s40, 0
	s_branch .LBB1_75
